# all small changes together: dead-row MFMA elision, loop back-edge bookkeeping moved in front of the barrier, gain/shift staging unroll, mod remainder-loop unroll, paired completion polls
# speedup vs baseline: 1.0086x; 1.0086x over previous
; __device__ __forceinline__ void phase_mod(const Ptrs& p, LAS unsigned char* lds) {
;     ...
; #pragma unroll 7
;             for (int k = kg; k < D; k += 42) { const f32x4 w = __builtin_nontemporal_load((const f32x4*)(wp + (size_t)k * NMOD)); a0 += w * sc[k]; a1 += w * sc[D + k]; }
.LBB0_16:
	global_load_dwordx4 v[100:103], v[20:21], off nt
	v_lshl_add_u64 v[20:21], v[20:21], 0, s[10:11]
	global_load_dwordx4 v[104:107], v[20:21], off nt
	v_lshl_add_u64 v[20:21], v[20:21], 0, s[10:11]
	global_load_dwordx4 v[108:111], v[20:21], off nt
	v_lshl_add_u64 v[20:21], v[20:21], 0, s[10:11]
	global_load_dwordx4 v[112:115], v[20:21], off nt
	v_lshl_add_u64 v[20:21], v[20:21], 0, s[10:11]
	global_load_dwordx4 v[116:119], v[20:21], off nt
	v_lshl_add_u64 v[20:21], v[20:21], 0, s[10:11]
	global_load_dwordx4 v[120:123], v[20:21], off nt
	v_lshl_add_u64 v[20:21], v[20:21], 0, s[10:11]
	ds_read2st64_b32 v[124:125], v22 offset1:32
	v_add_u32_e32 v22, 0xa8, v22
	ds_read2st64_b32 v[126:127], v22 offset1:32
	v_add_u32_e32 v22, 0xa8, v22
	ds_read2st64_b32 v[128:129], v22 offset1:32
	v_add_u32_e32 v22, 0xa8, v22
	ds_read2st64_b32 v[130:131], v22 offset1:32
	v_add_u32_e32 v22, 0xa8, v22
	ds_read2st64_b32 v[132:133], v22 offset1:32
	v_add_u32_e32 v22, 0xa8, v22
	ds_read2st64_b32 v[134:135], v22 offset1:32
	v_add_u32_e32 v22, 0xa8, v22
	v_add_u32_e32 v32, 0xfc, v32
	v_mov_b32_e32 v3, 0
	s_waitcnt lgkmcnt(0)
	s_waitcnt vmcnt(0)
	v_mov_b32_e32 v30, v125
	v_pk_fma_f32 v[6:7], v[102:103], v[124:125], v[6:7] op_sel_hi:[1,0,1]
	v_pk_fma_f32 v[4:5], v[100:101], v[124:125], v[4:5] op_sel_hi:[1,0,1]
	v_pk_fma_f32 v[10:11], v[102:103], v[30:31], v[10:11] op_sel_hi:[1,0,1]
	v_pk_fma_f32 v[8:9], v[100:101], v[30:31], v[8:9] op_sel_hi:[1,0,1]
	v_mov_b32_e32 v30, v127
	v_pk_fma_f32 v[6:7], v[106:107], v[126:127], v[6:7] op_sel_hi:[1,0,1]
	v_pk_fma_f32 v[4:5], v[104:105], v[126:127], v[4:5] op_sel_hi:[1,0,1]
	v_pk_fma_f32 v[10:11], v[106:107], v[30:31], v[10:11] op_sel_hi:[1,0,1]
	v_pk_fma_f32 v[8:9], v[104:105], v[30:31], v[8:9] op_sel_hi:[1,0,1]
	v_mov_b32_e32 v30, v129
	v_pk_fma_f32 v[6:7], v[110:111], v[128:129], v[6:7] op_sel_hi:[1,0,1]
	v_pk_fma_f32 v[4:5], v[108:109], v[128:129], v[4:5] op_sel_hi:[1,0,1]
	v_pk_fma_f32 v[10:11], v[110:111], v[30:31], v[10:11] op_sel_hi:[1,0,1]
	v_pk_fma_f32 v[8:9], v[108:109], v[30:31], v[8:9] op_sel_hi:[1,0,1]
	v_mov_b32_e32 v30, v131
	v_pk_fma_f32 v[6:7], v[114:115], v[130:131], v[6:7] op_sel_hi:[1,0,1]
	v_pk_fma_f32 v[4:5], v[112:113], v[130:131], v[4:5] op_sel_hi:[1,0,1]
	v_pk_fma_f32 v[10:11], v[114:115], v[30:31], v[10:11] op_sel_hi:[1,0,1]
	v_pk_fma_f32 v[8:9], v[112:113], v[30:31], v[8:9] op_sel_hi:[1,0,1]
	v_mov_b32_e32 v30, v133
	v_pk_fma_f32 v[6:7], v[118:119], v[132:133], v[6:7] op_sel_hi:[1,0,1]
	v_pk_fma_f32 v[4:5], v[116:117], v[132:133], v[4:5] op_sel_hi:[1,0,1]
	v_pk_fma_f32 v[10:11], v[118:119], v[30:31], v[10:11] op_sel_hi:[1,0,1]
	v_pk_fma_f32 v[8:9], v[116:117], v[30:31], v[8:9] op_sel_hi:[1,0,1]
	v_mov_b32_e32 v30, v135
	v_pk_fma_f32 v[6:7], v[122:123], v[134:135], v[6:7] op_sel_hi:[1,0,1]
	v_pk_fma_f32 v[4:5], v[120:121], v[134:135], v[4:5] op_sel_hi:[1,0,1]
	v_pk_fma_f32 v[10:11], v[122:123], v[30:31], v[10:11] op_sel_hi:[1,0,1]
	v_pk_fma_f32 v[8:9], v[120:121], v[30:31], v[8:9] op_sel_hi:[1,0,1]
	s_or_b64 exec, exec, s[20:21]

; #define LAS __attribute__((address_space(3)))
; #define G_DMA_A(buf, t, i_) __builtin_amdgcn_raw_ptr_buffer_load_lds(ra, (LAS void*)(lds + (buf) * 65536 + a_wu + (i_) * 8192), 16, ao##i_, (unsigned)(t) * 128u, 0, 0)
; #define G_ISSUE_B(t) do { const unsigned so_ = (unsigned)(t) * 64u * ldbB; _Pragma("unroll") for (int i_ = 0; i_ < 8; ++i_) sb[i_] = __builtin_bit_cast(f32x4, __builtin_amdgcn_raw_buffer_load_b128(rb, bo, so_ + (unsigned)i_ * ldbB, 0)); } while (0)
; #define G_RETIRE() asm volatile("s_waitcnt vmcnt(0)" : "+v"(sb[0]), "+v"(sb[1]), "+v"(sb[2]), "+v"(sb[3]), "+v"(sb[4]), "+v"(sb[5]), "+v"(sb[6]), "+v"(sb[7]) :: "memory")
; #define G_WRITE_B(buf) do { LAS unsigned char* d_ = lds + (buf) * 65536; \
;         _Pragma("unroll") for (int j_ = 0; j_ < 4; ++j_) { u32x4 w_; w_.x = cvtpk(sb[0][j_], sb[1][j_]); w_.y = cvtpk(sb[2][j_], sb[3][j_]); w_.z = cvtpk(sb[4][j_], sb[5][j_]); w_.w = cvtpk(sb[6][j_], sb[7][j_]); \
;             *(LAS u32x4*)(d_ + 32768 + T.b_w + ((T.b_rot + 64u * j_) & 255u)) = w_; } } while (0)
; #define G_BAR() do { asm volatile("s_waitcnt lgkmcnt(0)" ::: "memory"); __builtin_amdgcn_s_barrier(); asm volatile("" ::: "memory"); } while (0)
; __device__ __forceinline__ void gemm_kloop_light(f32x4 (&acc)[8][4], LAS unsigned char* lds, const GemmT& T, ...
;     ...
;     for (int t = 0; t < nt; ++t) { const int cur = t & 1; const bool w1 = t + 1 < nt, i2 = t + 2 < nt;
;         if (w1) { G_DMA_A(cur ^ 1, t + 1, 0); G_DMA_A(cur ^ 1, t + 1, 1); G_DMA_A(cur ^ 1, t + 1, 2); G_DMA_A(cur ^ 1, t + 1, 3); }
;         if (mlim > 0) {
; #pragma unroll
;             for (int ks = 0; ks < 2; ++ks) { const LAS unsigned char* s_ = lds + cur * 65536 + ks * 1024; bf16x8 Bf_[4];
; #pragma unroll
;                 for (int n_ = 0; n_ < 4; ++n_) Bf_[n_] = *(const LAS bf16x8*)(s_ + T.b_r + n_ * 2048);
; #pragma unroll
;                 for (int m_ = 0; m_ < 8; ++m_) if (m_ < mlim) { const bf16x8 At_ = *(const LAS bf16x8*)(s_ + T.a_r + m_ * 2048);
; #pragma unroll
;                     for (int n_ = 0; n_ < 4; ++n_) acc[m_][n_] = __builtin_amdgcn_mfma_f32_16x16x32_bf16(Bf_[n_], At_, acc[m_][n_], 0, 0, 0); } } }
;         if (w1) { G_RETIRE(); G_WRITE_B(cur ^ 1); }
;         if (i2) G_ISSUE_B(t + 2);
;         G_BAR(); }
.Lmy_d2g_bar:
	s_waitcnt lgkmcnt(0)
	s_add_i32 s69, s69, 0x80000
	s_add_i32 s68, s68, 0x10000
	s_addk_i32 s70, 0x80
	s_cmp_eq_u32 s69, 0x100e000
	s_barrier
	s_cbranch_scc1 .LBB0_1204

; #define G_DMA_A(buf, t, i_) __builtin_amdgcn_raw_ptr_buffer_load_lds(ra, (LAS void*)(lds + (buf) * 65536 + a_wu + (i_) * 8192), 16, ao##i_, (unsigned)(t) * 128u, 0, 0)
; #define G_ISSUE_B(t) do { const unsigned so_ = (unsigned)(t) * 64u * ldbB; _Pragma("unroll") for (int i_ = 0; i_ < 8; ++i_) sb[i_] = __builtin_bit_cast(f32x4, __builtin_amdgcn_raw_buffer_load_b128(rb, bo, so_ + (unsigned)i_ * ldbB, 0)); } while (0)
; #define G_RETIRE() asm volatile("s_waitcnt vmcnt(0)" : "+v"(sb[0]), "+v"(sb[1]), "+v"(sb[2]), "+v"(sb[3]), "+v"(sb[4]), "+v"(sb[5]), "+v"(sb[6]), "+v"(sb[7]) :: "memory")
; #define G_WRITE_B(buf) do { LAS unsigned char* d_ = lds + (buf) * 65536; \
;         _Pragma("unroll") for (int j_ = 0; j_ < 4; ++j_) { u32x4 w_; w_.x = cvtpk(sb[0][j_], sb[1][j_]); w_.y = cvtpk(sb[2][j_], sb[3][j_]); w_.z = cvtpk(sb[4][j_], sb[5][j_]); w_.w = cvtpk(sb[6][j_], sb[7][j_]); \
;             *(LAS u32x4*)(d_ + 32768 + T.b_w + ((T.b_rot + 64u * j_) & 255u)) = w_; } } while (0)
; #define G_LDB(dst, buf, ks) do { const LAS unsigned char* s_ = lds + (buf) * 65536 + (ks) * 1024; _Pragma("unroll") for (int n_ = 0; n_ < 4; ++n_) dst[n_] = *(const LAS bf16x8*)(s_ + T.b_r + n_ * 2048); } while (0)
; #define G_LDA(dst, buf, ks, h_) do { const LAS unsigned char* s_ = lds + (buf) * 65536 + (ks) * 1024; _Pragma("unroll") for (int m_ = 0; m_ < 4; ++m_) dst[m_] = *(const LAS bf16x8*)(s_ + T.a_r + ((h_) * 4 + m_) * 2048); } while (0)
; #define G_SB() __builtin_amdgcn_sched_barrier(0)
; #define G_BAR() do { asm volatile("s_waitcnt lgkmcnt(0)" ::: "memory"); __builtin_amdgcn_s_barrier(); asm volatile("" ::: "memory"); } while (0)
; __device__ __forceinline__ void gemm_kloop(f32x4 (&acc)[8][4], LAS unsigned char* lds, const GemmT& T, ...
;     ...
;     for (int t = 0; t < nt; ++t) { const int cur = t & 1; const bool w1 = t + 1 < nt, i2 = t + 2 < nt;
;         G_LDB(Bf0, cur, 0); G_LDA(AtA, cur, 0, 0); G_SB();
;         G_LDA(AtB, cur, 0, 1); if (w1) { G_DMA_A(cur ^ 1, t + 1, 0); G_DMA_A(cur ^ 1, t + 1, 1); G_DMA_A(cur ^ 1, t + 1, 2); G_DMA_A(cur ^ 1, t + 1, 3); } G_MMA(AtA, Bf0, 0); G_SB();
;         G_LDB(Bf1, cur, 1); G_LDA(AtA, cur, 1, 0); G_MMA(AtB, Bf0, 1); G_SB();
;         G_LDA(AtB, cur, 1, 1); if (w1) { G_RETIRE(); G_WRITE_B(cur ^ 1); } if (i2) G_ISSUE_B(t + 2); G_MMA(AtA, Bf1, 0); G_SB();
;         G_MMA(AtB, Bf1, 1); G_SB();
;         G_BAR(); }
.Lmy_elgc:
	s_waitcnt vmcnt(0)
	s_add_i32 s7, s4, 0xffff2000
	s_waitcnt lgkmcnt(3)
	v_mfma_f32_16x16x32_bf16 v[160:163], v[164:167], v[176:179], v[160:163]
	v_cvt_pk_bf16_f32 v228, v5, v9
	v_cvt_pk_bf16_f32 v232, v6, v10
	s_add_i32 s8, s4, 0xffff4000
	v_mfma_f32_16x16x32_bf16 v[156:159], v[168:171], v[176:179], v[156:159]
	v_cvt_pk_bf16_f32 v229, v13, v17
	v_cvt_pk_bf16_f32 v233, v14, v18
	v_cvt_pk_bf16_f32 v230, v21, v29
	v_mfma_f32_16x16x32_bf16 v[152:155], v[180:183], v[176:179], v[152:155]
	v_cvt_pk_bf16_f32 v234, v22, v30
	v_cvt_pk_bf16_f32 v231, v25, v33
	v_cvt_pk_bf16_f32 v235, v26, v34
	v_mfma_f32_16x16x32_bf16 v[148:151], v[184:187], v[176:179], v[148:151]
	v_cvt_pk_bf16_f32 v172, v4, v8
	v_cvt_pk_bf16_f32 v173, v12, v16
	v_cvt_pk_bf16_f32 v174, v20, v28
	s_waitcnt lgkmcnt(2)
	v_mfma_f32_16x16x32_bf16 v[144:147], v[164:167], v[200:203], v[144:147]
	v_cvt_pk_bf16_f32 v175, v24, v32
	v_add_u32_e32 v3, s6, v227
	v_mfma_f32_16x16x32_bf16 v[140:143], v[168:171], v[200:203], v[140:143]
	v_mfma_f32_16x16x32_bf16 v[136:139], v[180:183], v[200:203], v[136:139]
	v_mfma_f32_16x16x32_bf16 v[132:135], v[184:187], v[200:203], v[132:135]
	v_cvt_pk_bf16_f32 v188, v7, v11
	buffer_load_dwordx4 v[4:7], v225, s[24:27], s7 offen
	buffer_load_dwordx4 v[8:11], v225, s[24:27], s8 offen
	s_add_i32 s7, s4, 0xffff6000
	v_cvt_pk_bf16_f32 v189, v15, v19
	s_add_i32 s8, s4, 0xffff8000
	buffer_load_dwordx4 v[12:15], v225, s[24:27], s7 offen
	buffer_load_dwordx4 v[16:19], v225, s[24:27], s8 offen
	s_add_i32 s7, s4, 0xffffa000
	v_cvt_pk_bf16_f32 v190, v23, v31
	s_add_i32 s8, s4, 0xffffc000
	buffer_load_dwordx4 v[20:23], v225, s[24:27], s7 offen
	buffer_load_dwordx4 v[28:31], v225, s[24:27], s8 offen
	s_add_i32 s7, s4, 0xffffe000
	v_cvt_pk_bf16_f32 v191, v27, v35
	buffer_load_dwordx4 v[24:27], v225, s[24:27], s7 offen
	buffer_load_dwordx4 v[32:35], v225, s[24:27], s4 offen
	s_waitcnt lgkmcnt(1)
	v_mfma_f32_16x16x32_bf16 v[128:131], v[164:167], v[204:207], v[128:131]
	v_mfma_f32_16x16x32_bf16 v[124:127], v[168:171], v[204:207], v[124:127]
	v_mfma_f32_16x16x32_bf16 v[120:123], v[180:183], v[204:207], v[120:123]
	v_mfma_f32_16x16x32_bf16 v[116:119], v[184:187], v[204:207], v[116:119]
	v_add_u32_e32 v192, v3, v220
	v_add_u32_e32 v3, v3, v218
	ds_write_b128 v192, v[172:175] offset:32768
	ds_write_b128 v192, v[228:231] offset:32832
	s_waitcnt lgkmcnt(2)
	v_mfma_f32_16x16x32_bf16 v[112:115], v[164:167], v[208:211], v[112:115]
	ds_write_b128 v192, v[232:235] offset:32896
	ds_write_b128 v3, v[188:191] offset:32768
	v_mfma_f32_16x16x32_bf16 v[108:111], v[168:171], v[208:211], v[108:111]
	v_mfma_f32_16x16x32_bf16 v[104:107], v[180:183], v[208:211], v[104:107]
	v_mfma_f32_16x16x32_bf16 v[100:103], v[184:187], v[208:211], v[100:103]
	s_waitcnt lgkmcnt(0)
	s_add_i32 s4, s4, 0x80000
	s_addk_i32 s5, 0x80
	s_add_i32 s3, s3, 0x10000
	s_cmp_lg_u32 s4, 0x100e000
	s_barrier
	s_cbranch_scc1 .LBB0_1265
	v_add_u32_e32 v3, 0, v226
	v_add_u32_e32 v204, 0, v216
	ds_read_b128 v[164:167], v3 offset:32768
	ds_read_b128 v[168:171], v3 offset:34816
	ds_read_b128 v[172:175], v3 offset:36864
	ds_read_b128 v[176:179], v3 offset:38912
	ds_read_b128 v[180:183], v204
	ds_read_b128 v[184:187], v204 offset:2048
	ds_read_b128 v[188:191], v204 offset:4096
	ds_read_b128 v[192:195], v204 offset:6144
	s_add_i32 m0, s1, 0x10000
	s_add_i32 s3, s1, 0x16000
	s_add_i32 s4, s1, 0x14000
	s_add_i32 s1, s1, 0x12000
	s_mov_b32 s38, s26
	s_mov_b32 s39, s27
	s_waitcnt lgkmcnt(3)
	v_mfma_f32_16x16x32_bf16 v[160:163], v[164:167], v[180:183], v[160:163]
	v_mfma_f32_16x16x32_bf16 v[156:159], v[168:171], v[180:183], v[156:159]
	v_mfma_f32_16x16x32_bf16 v[152:155], v[172:175], v[180:183], v[152:155]
	v_mfma_f32_16x16x32_bf16 v[148:151], v[176:179], v[180:183], v[148:151]
	s_waitcnt lgkmcnt(2)
	v_mfma_f32_16x16x32_bf16 v[144:147], v[164:167], v[184:187], v[144:147]
	v_mfma_f32_16x16x32_bf16 v[140:143], v[168:171], v[184:187], v[140:143]
	v_mfma_f32_16x16x32_bf16 v[136:139], v[172:175], v[184:187], v[136:139]
	v_mfma_f32_16x16x32_bf16 v[132:135], v[176:179], v[184:187], v[132:135]
	ds_read_b128 v[180:183], v204 offset:8192
	ds_read_b128 v[184:187], v204 offset:10240
	ds_read_b128 v[196:199], v204 offset:12288
	ds_read_b128 v[200:203], v204 offset:14336
	buffer_load_dwordx4 v223, s[36:39], s83 offen lds
	s_mov_b32 m0, s1
	s_waitcnt lgkmcnt(4)
	v_mfma_f32_16x16x32_bf16 v[112:115], v[164:167], v[192:195], v[112:115]
	buffer_load_dwordx4 v222, s[36:39], s83 offen lds
	s_mov_b32 m0, s4
	s_nop 0
	buffer_load_dwordx4 v221, s[36:39], s83 offen lds
	s_mov_b32 m0, s3
	v_mfma_f32_16x16x32_bf16 v[108:111], v[168:171], v[192:195], v[108:111]
	buffer_load_dwordx4 v224, s[36:39], s83 offen lds
	v_mfma_f32_16x16x32_bf16 v[104:107], v[172:175], v[192:195], v[104:107]
	v_mfma_f32_16x16x32_bf16 v[100:103], v[176:179], v[192:195], v[100:103]
	v_mfma_f32_16x16x32_bf16 v[128:131], v[164:167], v[188:191], v[128:131]
	v_mfma_f32_16x16x32_bf16 v[124:127], v[168:171], v[188:191], v[124:127]
	v_mfma_f32_16x16x32_bf16 v[120:123], v[172:175], v[188:191], v[120:123]
	v_mfma_f32_16x16x32_bf16 v[116:119], v[176:179], v[188:191], v[116:119]
	s_waitcnt lgkmcnt(3)
	v_mfma_f32_16x16x32_bf16 v[96:99], v[164:167], v[180:183], v[96:99]
	v_mfma_f32_16x16x32_bf16 v[92:95], v[168:171], v[180:183], v[92:95]
	v_mfma_f32_16x16x32_bf16 v[88:91], v[172:175], v[180:183], v[88:91]
	v_mfma_f32_16x16x32_bf16 v[84:87], v[176:179], v[180:183], v[84:87]
	s_waitcnt lgkmcnt(2)
	v_mfma_f32_16x16x32_bf16 v[80:83], v[164:167], v[184:187], v[80:83]
	v_mfma_f32_16x16x32_bf16 v[76:79], v[168:171], v[184:187], v[76:79]
	v_mfma_f32_16x16x32_bf16 v[72:75], v[172:175], v[184:187], v[72:75]
	v_mfma_f32_16x16x32_bf16 v[68:71], v[176:179], v[184:187], v[68:71]
	s_waitcnt lgkmcnt(1)
; #define G_DMA_A(buf, t, i_) __builtin_amdgcn_raw_ptr_buffer_load_lds(ra, (LAS void*)(lds + (buf) * 65536 + a_wu + (i_) * 8192), 16, ao##i_, (unsigned)(t) * 128u, 0, 0)
; #define G_ISSUE_B(t) do { const unsigned so_ = (unsigned)(t) * 64u * ldbB; _Pragma("unroll") for (int i_ = 0; i_ < 8; ++i_) sb[i_] = __builtin_bit_cast(f32x4, __builtin_amdgcn_raw_buffer_load_b128(rb, bo, so_ + (unsigned)i_ * ldbB, 0)); } while (0)
; #define G_RETIRE() asm volatile("s_waitcnt vmcnt(0)" : "+v"(sb[0]), "+v"(sb[1]), "+v"(sb[2]), "+v"(sb[3]), "+v"(sb[4]), "+v"(sb[5]), "+v"(sb[6]), "+v"(sb[7]) :: "memory")
; #define G_WRITE_B(buf) do { LAS unsigned char* d_ = lds + (buf) * 65536; \
;         _Pragma("unroll") for (int j_ = 0; j_ < 4; ++j_) { u32x4 w_; w_.x = cvtpk(sb[0][j_], sb[1][j_]); w_.y = cvtpk(sb[2][j_], sb[3][j_]); w_.z = cvtpk(sb[4][j_], sb[5][j_]); w_.w = cvtpk(sb[6][j_], sb[7][j_]); \
;             *(LAS u32x4*)(d_ + 32768 + T.b_w + ((T.b_rot + 64u * j_) & 255u)) = w_; } } while (0)
; #define G_LDB(dst, buf, ks) do { const LAS unsigned char* s_ = lds + (buf) * 65536 + (ks) * 1024; _Pragma("unroll") for (int n_ = 0; n_ < 4; ++n_) dst[n_] = *(const LAS bf16x8*)(s_ + T.b_r + n_ * 2048); } while (0)
; #define G_LDA(dst, buf, ks, h_) do { const LAS unsigned char* s_ = lds + (buf) * 65536 + (ks) * 1024; _Pragma("unroll") for (int m_ = 0; m_ < 4; ++m_) dst[m_] = *(const LAS bf16x8*)(s_ + T.a_r + ((h_) * 4 + m_) * 2048); } while (0)
; #define G_SB() __builtin_amdgcn_sched_barrier(0)
; #define G_BAR() do { asm volatile("s_waitcnt lgkmcnt(0)" ::: "memory"); __builtin_amdgcn_s_barrier(); asm volatile("" ::: "memory"); } while (0)
; __device__ __forceinline__ void gemm_kloop(f32x4 (&acc)[8][4], LAS unsigned char* lds, const GemmT& T, ...
;     ...
;     for (int t = 0; t < nt; ++t) { const int cur = t & 1; const bool w1 = t + 1 < nt, i2 = t + 2 < nt;
;         G_LDB(Bf0, cur, 0); G_LDA(AtA, cur, 0, 0); G_SB();
;         G_LDA(AtB, cur, 0, 1); if (w1) { G_DMA_A(cur ^ 1, t + 1, 0); G_DMA_A(cur ^ 1, t + 1, 1); G_DMA_A(cur ^ 1, t + 1, 2); G_DMA_A(cur ^ 1, t + 1, 3); } G_MMA(AtA, Bf0, 0); G_SB();
;         G_LDB(Bf1, cur, 1); G_LDA(AtA, cur, 1, 0); G_MMA(AtB, Bf0, 1); G_SB();
;         G_LDA(AtB, cur, 1, 1); if (w1) { G_RETIRE(); G_WRITE_B(cur ^ 1); } if (i2) G_ISSUE_B(t + 2); G_MMA(AtA, Bf1, 0); G_SB();
;         G_MMA(AtB, Bf1, 1); G_SB();
;         G_BAR(); }
	v_mfma_f32_16x16x32_bf16 v[64:67], v[164:167], v[196:199], v[64:67]
	v_mfma_f32_16x16x32_bf16 v[60:63], v[168:171], v[196:199], v[60:63]
	v_mfma_f32_16x16x32_bf16 v[56:59], v[172:175], v[196:199], v[56:59]
	v_mfma_f32_16x16x32_bf16 v[52:55], v[176:179], v[196:199], v[52:55]
	s_waitcnt lgkmcnt(0)
	v_mfma_f32_16x16x32_bf16 v[48:51], v[164:167], v[200:203], v[48:51]
	v_mfma_f32_16x16x32_bf16 v[44:47], v[168:171], v[200:203], v[44:47]
	ds_read_b128 v[164:167], v3 offset:33792
	ds_read_b128 v[168:171], v3 offset:35840
	ds_read_b128 v[180:183], v3 offset:37888
	ds_read_b128 v[184:187], v3 offset:39936
	v_mfma_f32_16x16x32_bf16 v[40:43], v[172:175], v[200:203], v[40:43]
	ds_read_b128 v[172:175], v204 offset:1024
	ds_read_b128 v[188:191], v204 offset:3072
	ds_read_b128 v[192:195], v204 offset:5120
	ds_read_b128 v[196:199], v204 offset:7168
	v_mfma_f32_16x16x32_bf16 v[36:39], v[176:179], v[200:203], v[36:39]
	s_waitcnt lgkmcnt(3)
	v_mfma_f32_16x16x32_bf16 v[160:163], v[164:167], v[172:175], v[160:163]
	v_add_u32_e32 v3, s29, v219
	v_mfma_f32_16x16x32_bf16 v[156:159], v[168:171], v[172:175], v[156:159]
	v_mfma_f32_16x16x32_bf16 v[152:155], v[180:183], v[172:175], v[152:155]
	v_mfma_f32_16x16x32_bf16 v[148:151], v[184:187], v[172:175], v[148:151]
	ds_read_b128 v[172:175], v204 offset:9216
	ds_read_b128 v[176:179], v204 offset:11264
	ds_read_b128 v[200:203], v204 offset:13312
	ds_read_b128 v[204:207], v204 offset:15360
	s_waitcnt vmcnt(4)
	s_waitcnt vmcnt(0)
	s_waitcnt lgkmcnt(6)
	v_mfma_f32_16x16x32_bf16 v[144:147], v[164:167], v[188:191], v[144:147]
	v_mfma_f32_16x16x32_bf16 v[140:143], v[168:171], v[188:191], v[140:143]
	v_mfma_f32_16x16x32_bf16 v[136:139], v[180:183], v[188:191], v[136:139]
	v_mfma_f32_16x16x32_bf16 v[132:135], v[184:187], v[188:191], v[132:135]
	v_cvt_pk_bf16_f32 v188, v4, v8
	v_cvt_pk_bf16_f32 v189, v12, v16
	v_cvt_pk_bf16_f32 v190, v20, v28
	v_cvt_pk_bf16_f32 v191, v24, v32
	v_add_u32_e32 v4, v3, v220
	ds_write_b128 v4, v[188:191]
	v_cvt_pk_bf16_f32 v188, v5, v9
	v_cvt_pk_bf16_f32 v189, v13, v17
	v_cvt_pk_bf16_f32 v190, v21, v29
	v_cvt_pk_bf16_f32 v191, v25, v33
	ds_write_b128 v4, v[188:191] offset:64
	v_cvt_pk_bf16_f32 v188, v6, v10
	v_cvt_pk_bf16_f32 v189, v14, v18
	v_cvt_pk_bf16_f32 v190, v22, v30
	v_cvt_pk_bf16_f32 v191, v26, v34
	ds_write_b128 v4, v[188:191] offset:128
	v_cvt_pk_bf16_f32 v4, v7, v11
	v_cvt_pk_bf16_f32 v5, v15, v19
	v_cvt_pk_bf16_f32 v6, v23, v31
	v_cvt_pk_bf16_f32 v7, v27, v35
	v_add_u32_e32 v3, v3, v218
	s_waitcnt lgkmcnt(7)
	v_mfma_f32_16x16x32_bf16 v[112:115], v[164:167], v[196:199], v[112:115]
	ds_write_b128 v3, v[4:7]
	v_mfma_f32_16x16x32_bf16 v[108:111], v[168:171], v[196:199], v[108:111]
	v_mfma_f32_16x16x32_bf16 v[8:11], v[180:183], v[196:199], v[104:107]
	v_mfma_f32_16x16x32_bf16 v[4:7], v[184:187], v[196:199], v[100:103]
	v_mfma_f32_16x16x32_bf16 v[128:131], v[164:167], v[192:195], v[128:131]
	v_mfma_f32_16x16x32_bf16 v[124:127], v[168:171], v[192:195], v[124:127]
	v_mfma_f32_16x16x32_bf16 v[120:123], v[180:183], v[192:195], v[120:123]
	v_mfma_f32_16x16x32_bf16 v[116:119], v[184:187], v[192:195], v[116:119]
	s_waitcnt lgkmcnt(7)
	v_mfma_f32_16x16x32_bf16 v[12:15], v[164:167], v[172:175], v[96:99]
	v_mfma_f32_16x16x32_bf16 v[16:19], v[168:171], v[172:175], v[92:95]
	v_mfma_f32_16x16x32_bf16 v[20:23], v[180:183], v[172:175], v[88:91]
	v_mfma_f32_16x16x32_bf16 v[24:27], v[184:187], v[172:175], v[84:87]
	s_waitcnt lgkmcnt(6)
	v_mfma_f32_16x16x32_bf16 v[28:31], v[164:167], v[176:179], v[80:83]
	v_mfma_f32_16x16x32_bf16 v[32:35], v[168:171], v[176:179], v[76:79]
	v_mfma_f32_16x16x32_bf16 v[72:75], v[180:183], v[176:179], v[72:75]
	v_mfma_f32_16x16x32_bf16 v[68:71], v[184:187], v[176:179], v[68:71]
	s_waitcnt lgkmcnt(5)
	v_mfma_f32_16x16x32_bf16 v[64:67], v[164:167], v[200:203], v[64:67]
	v_mfma_f32_16x16x32_bf16 v[60:63], v[168:171], v[200:203], v[60:63]
	v_mfma_f32_16x16x32_bf16 v[56:59], v[180:183], v[200:203], v[56:59]
	v_mfma_f32_16x16x32_bf16 v[52:55], v[184:187], v[200:203], v[52:55]
	s_waitcnt lgkmcnt(4)
	v_mfma_f32_16x16x32_bf16 v[48:51], v[164:167], v[204:207], v[48:51]
	v_mfma_f32_16x16x32_bf16 v[44:47], v[168:171], v[204:207], v[44:47]
	v_mfma_f32_16x16x32_bf16 v[40:43], v[180:183], v[204:207], v[40:43]
	v_mfma_f32_16x16x32_bf16 v[36:39], v[184:187], v[204:207], v[36:39]
	s_add_i32 s1, 0, 0x10000
	s_waitcnt lgkmcnt(0)
	s_barrier
; #define G_DMA_A(buf, t, i_) __builtin_amdgcn_raw_ptr_buffer_load_lds(ra, (LAS void*)(lds + (buf) * 65536 + a_wu + (i_) * 8192), 16, ao##i_, (unsigned)(t) * 128u, 0, 0)
; #define G_ISSUE_B(t) do { const unsigned so_ = (unsigned)(t) * 64u * ldbB; _Pragma("unroll") for (int i_ = 0; i_ < 8; ++i_) sb[i_] = __builtin_bit_cast(f32x4, __builtin_amdgcn_raw_buffer_load_b128(rb, bo, so_ + (unsigned)i_ * ldbB, 0)); } while (0)
; #define G_RETIRE() asm volatile("s_waitcnt vmcnt(0)" : "+v"(sb[0]), "+v"(sb[1]), "+v"(sb[2]), "+v"(sb[3]), "+v"(sb[4]), "+v"(sb[5]), "+v"(sb[6]), "+v"(sb[7]) :: "memory")
; #define G_WRITE_B(buf) do { LAS unsigned char* d_ = lds + (buf) * 65536; \
;         _Pragma("unroll") for (int j_ = 0; j_ < 4; ++j_) { u32x4 w_; w_.x = cvtpk(sb[0][j_], sb[1][j_]); w_.y = cvtpk(sb[2][j_], sb[3][j_]); w_.z = cvtpk(sb[4][j_], sb[5][j_]); w_.w = cvtpk(sb[6][j_], sb[7][j_]); \
;             *(LAS u32x4*)(d_ + 32768 + T.b_w + ((T.b_rot + 64u * j_) & 255u)) = w_; } } while (0)
; #define G_LDB(dst, buf, ks) do { const LAS unsigned char* s_ = lds + (buf) * 65536 + (ks) * 1024; _Pragma("unroll") for (int n_ = 0; n_ < 4; ++n_) dst[n_] = *(const LAS bf16x8*)(s_ + T.b_r + n_ * 2048); } while (0)
; #define G_LDA(dst, buf, ks, h_) do { const LAS unsigned char* s_ = lds + (buf) * 65536 + (ks) * 1024; _Pragma("unroll") for (int m_ = 0; m_ < 4; ++m_) dst[m_] = *(const LAS bf16x8*)(s_ + T.a_r + ((h_) * 4 + m_) * 2048); } while (0)
; #define G_SB() __builtin_amdgcn_sched_barrier(0)
; #define G_BAR() do { asm volatile("s_waitcnt lgkmcnt(0)" ::: "memory"); __builtin_amdgcn_s_barrier(); asm volatile("" ::: "memory"); } while (0)
; __device__ __forceinline__ void gemm_kloop(f32x4 (&acc)[8][4], LAS unsigned char* lds, const GemmT& T, ...
;     ...
;     for (int t = 0; t < nt; ++t) { const int cur = t & 1; const bool w1 = t + 1 < nt, i2 = t + 2 < nt;
;         G_LDB(Bf0, cur, 0); G_LDA(AtA, cur, 0, 0); G_SB();
;         G_LDA(AtB, cur, 0, 1); if (w1) { G_DMA_A(cur ^ 1, t + 1, 0); G_DMA_A(cur ^ 1, t + 1, 1); G_DMA_A(cur ^ 1, t + 1, 2); G_DMA_A(cur ^ 1, t + 1, 3); } G_MMA(AtA, Bf0, 0); G_SB();
;         G_LDB(Bf1, cur, 1); G_LDA(AtA, cur, 1, 0); G_MMA(AtB, Bf0, 1); G_SB();
;         G_LDA(AtB, cur, 1, 1); if (w1) { G_RETIRE(); G_WRITE_B(cur ^ 1); } if (i2) G_ISSUE_B(t + 2); G_MMA(AtA, Bf1, 0); G_SB();
;         G_MMA(AtB, Bf1, 1); G_SB();
;         G_BAR(); }
	v_add_u32_e32 v3, s1, v217
	ds_read_b128 v[76:79], v3
	ds_read_b128 v[80:83], v3 offset:2048
	ds_read_b128 v[84:87], v3 offset:4096
	ds_read_b128 v[88:91], v3 offset:6144
	v_add_u32_e32 v3, s1, v216
	ds_read_b128 v[92:95], v3
	ds_read_b128 v[96:99], v3 offset:2048
	ds_read_b128 v[100:103], v3 offset:4096
	ds_read_b128 v[104:107], v3 offset:6144
	s_waitcnt lgkmcnt(2)
	v_mfma_f32_16x16x32_bf16 v[144:147], v[76:79], v[96:99], v[144:147]
	v_mfma_f32_16x16x32_bf16 v[140:143], v[80:83], v[96:99], v[140:143]
	v_mfma_f32_16x16x32_bf16 v[172:175], v[84:87], v[96:99], v[136:139]
	v_mfma_f32_16x16x32_bf16 v[96:99], v[88:91], v[96:99], v[132:135]
	s_waitcnt lgkmcnt(1)
	v_mfma_f32_16x16x32_bf16 v[128:131], v[76:79], v[100:103], v[128:131]
	v_mfma_f32_16x16x32_bf16 v[124:127], v[80:83], v[100:103], v[124:127]
	v_mfma_f32_16x16x32_bf16 v[120:123], v[84:87], v[100:103], v[120:123]
	v_mfma_f32_16x16x32_bf16 v[116:119], v[88:91], v[100:103], v[116:119]
	s_waitcnt lgkmcnt(0)
	v_mfma_f32_16x16x32_bf16 v[132:135], v[76:79], v[104:107], v[112:115]
	v_mfma_f32_16x16x32_bf16 v[176:179], v[80:83], v[104:107], v[108:111]
	ds_read_b128 v[100:103], v3 offset:8192
	s_nop 1
	ds_read_b128 v[108:111], v3 offset:10240
	ds_read_b128 v[112:115], v3 offset:12288
	ds_read_b128 v[136:139], v3 offset:14336
	v_mfma_f32_16x16x32_bf16 v[160:163], v[76:79], v[92:95], v[160:163]
	v_mfma_f32_16x16x32_bf16 v[164:167], v[80:83], v[92:95], v[156:159]
	v_mfma_f32_16x16x32_bf16 v[168:171], v[84:87], v[92:95], v[152:155]
	v_mfma_f32_16x16x32_bf16 v[92:95], v[88:91], v[92:95], v[148:151]
	v_mfma_f32_16x16x32_bf16 v[8:11], v[84:87], v[104:107], v[8:11]
	v_mfma_f32_16x16x32_bf16 v[4:7], v[88:91], v[104:107], v[4:7]
	v_add_u32_e32 v3, s64, v217
	ds_read_b128 v[218:221], v3
	ds_read_b128 v[222:225], v3 offset:2048
	ds_read_b128 v[230:233], v3 offset:4096
	ds_read_b128 v[234:237], v3 offset:6144
	v_add_u32_e32 v3, s64, v216
	s_waitcnt lgkmcnt(5)
	v_mfma_f32_16x16x32_bf16 v[206:209], v[88:91], v[112:115], v[52:55]
	s_waitcnt lgkmcnt(4)
	v_mfma_f32_16x16x32_bf16 v[210:213], v[76:79], v[136:139], v[48:51]
	v_mfma_f32_16x16x32_bf16 v[226:229], v[80:83], v[136:139], v[44:47]
	v_mfma_f32_16x16x32_bf16 v[238:241], v[84:87], v[136:139], v[40:43]
	s_nop 2
	ds_read_b128 v[40:43], v3
	ds_read_b128 v[44:47], v3 offset:2048
	ds_read_b128 v[48:51], v3 offset:4096
	ds_read_b128 v[52:55], v3 offset:6144
	v_mfma_f32_16x16x32_bf16 v[12:15], v[76:79], v[100:103], v[12:15]
	v_mfma_f32_16x16x32_bf16 v[16:19], v[80:83], v[100:103], v[16:19]
	v_mfma_f32_16x16x32_bf16 v[20:23], v[84:87], v[100:103], v[20:23]
	v_mfma_f32_16x16x32_bf16 v[24:27], v[88:91], v[100:103], v[24:27]
	v_mfma_f32_16x16x32_bf16 v[28:31], v[76:79], v[108:111], v[28:31]
	v_mfma_f32_16x16x32_bf16 v[32:35], v[80:83], v[108:111], v[32:35]
	v_mfma_f32_16x16x32_bf16 v[180:183], v[84:87], v[108:111], v[72:75]
	v_mfma_f32_16x16x32_bf16 v[184:187], v[88:91], v[108:111], v[68:71]
	v_mfma_f32_16x16x32_bf16 v[188:191], v[76:79], v[112:115], v[64:67]
	v_mfma_f32_16x16x32_bf16 v[198:201], v[80:83], v[112:115], v[60:63]
	v_mfma_f32_16x16x32_bf16 v[202:205], v[84:87], v[112:115], v[56:59]
	v_mfma_f32_16x16x32_bf16 v[242:245], v[88:91], v[136:139], v[36:39]
	s_waitcnt lgkmcnt(3)
	v_mfma_f32_16x16x32_bf16 v[154:157], v[218:221], v[40:43], v[160:163]
	v_mfma_f32_16x16x32_bf16 v[158:161], v[234:237], v[40:43], v[92:95]
	s_waitcnt lgkmcnt(2)
	v_mfma_f32_16x16x32_bf16 v[106:109], v[218:221], v[44:47], v[144:147]
	v_mfma_f32_16x16x32_bf16 v[138:141], v[222:225], v[44:47], v[140:143]
	v_mfma_f32_16x16x32_bf16 v[102:105], v[230:233], v[44:47], v[172:175]
	v_mfma_f32_16x16x32_bf16 v[110:113], v[234:237], v[44:47], v[96:99]
	s_waitcnt lgkmcnt(1)
	v_mfma_f32_16x16x32_bf16 v[90:93], v[218:221], v[48:51], v[128:131]
	v_mfma_f32_16x16x32_bf16 v[98:101], v[222:225], v[48:51], v[124:127]
	v_mfma_f32_16x16x32_bf16 v[86:89], v[230:233], v[48:51], v[120:123]
	v_mfma_f32_16x16x32_bf16 v[94:97], v[234:237], v[48:51], v[116:119]
	s_waitcnt lgkmcnt(0)
	v_mfma_f32_16x16x32_bf16 v[70:73], v[230:233], v[52:55], v[8:11]
	s_nop 2
	ds_read_b128 v[8:11], v3 offset:8192
	ds_read_b128 v[46:49], v3 offset:10240
	ds_read_b128 v[114:117], v3 offset:12288
	ds_read_b128 v[118:121], v3 offset:14336
	v_mfma_f32_16x16x32_bf16 v[194:197], v[222:225], v[40:43], v[164:167]
	v_mfma_f32_16x16x32_bf16 v[150:153], v[230:233], v[40:43], v[168:171]
	v_mfma_f32_16x16x32_bf16 v[74:77], v[218:221], v[52:55], v[132:135]
	v_mfma_f32_16x16x32_bf16 v[82:85], v[222:225], v[52:55], v[176:179]
	v_mfma_f32_16x16x32_bf16 v[78:81], v[234:237], v[52:55], v[4:7]
	s_waitcnt lgkmcnt(3)
	v_mfma_f32_16x16x32_bf16 v[58:61], v[218:221], v[8:11], v[12:15]
	v_mfma_f32_16x16x32_bf16 v[66:69], v[222:225], v[8:11], v[16:19]
	v_mfma_f32_16x16x32_bf16 v[54:57], v[230:233], v[8:11], v[20:23]
	v_mfma_f32_16x16x32_bf16 v[62:65], v[234:237], v[8:11], v[24:27]
	s_waitcnt lgkmcnt(2)
	v_mfma_f32_16x16x32_bf16 v[42:45], v[218:221], v[46:49], v[28:31]
	v_mfma_f32_16x16x32_bf16 v[50:53], v[222:225], v[46:49], v[32:35]
	v_mfma_f32_16x16x32_bf16 v[38:41], v[230:233], v[46:49], v[180:183]
	v_mfma_f32_16x16x32_bf16 v[46:49], v[234:237], v[46:49], v[184:187]
	s_waitcnt lgkmcnt(1)
	v_mfma_f32_16x16x32_bf16 v[26:29], v[218:221], v[114:117], v[188:191]
	v_mfma_f32_16x16x32_bf16 v[34:37], v[222:225], v[114:117], v[198:201]
	v_mfma_f32_16x16x32_bf16 v[22:25], v[230:233], v[114:117], v[202:205]
	v_mfma_f32_16x16x32_bf16 v[30:33], v[234:237], v[114:117], v[206:209]
	s_waitcnt lgkmcnt(0)
	v_mfma_f32_16x16x32_bf16 v[10:13], v[218:221], v[118:121], v[210:213]
	v_mfma_f32_16x16x32_bf16 v[18:21], v[222:225], v[118:121], v[226:229]
	v_mfma_f32_16x16x32_bf16 v[6:9], v[230:233], v[118:121], v[238:241]
	v_mfma_f32_16x16x32_bf16 v[14:17], v[234:237], v[118:121], v[242:245]
	s_waitcnt lgkmcnt(0)
	s_barrier

; #define LAS __attribute__((address_space(3)))
; #define G_DMA_A(buf, t, i_) __builtin_amdgcn_raw_ptr_buffer_load_lds(ra, (LAS void*)(lds + (buf) * 65536 + a_wu + (i_) * 8192), 16, ao##i_, (unsigned)(t) * 128u, 0, 0)
; #define G_ISSUE_B(t) do { const unsigned so_ = (unsigned)(t) * 64u * ldbB; _Pragma("unroll") for (int i_ = 0; i_ < 8; ++i_) sb[i_] = __builtin_bit_cast(f32x4, __builtin_amdgcn_raw_buffer_load_b128(rb, bo, so_ + (unsigned)i_ * ldbB, 0)); } while (0)
; #define G_RETIRE() asm volatile("s_waitcnt vmcnt(0)" : "+v"(sb[0]), "+v"(sb[1]), "+v"(sb[2]), "+v"(sb[3]), "+v"(sb[4]), "+v"(sb[5]), "+v"(sb[6]), "+v"(sb[7]) :: "memory")
; #define G_WRITE_B(buf) do { LAS unsigned char* d_ = lds + (buf) * 65536; \
;         _Pragma("unroll") for (int j_ = 0; j_ < 4; ++j_) { u32x4 w_; w_.x = cvtpk(sb[0][j_], sb[1][j_]); w_.y = cvtpk(sb[2][j_], sb[3][j_]); w_.z = cvtpk(sb[4][j_], sb[5][j_]); w_.w = cvtpk(sb[6][j_], sb[7][j_]); \
;             *(LAS u32x4*)(d_ + 32768 + T.b_w + ((T.b_rot + 64u * j_) & 255u)) = w_; } } while (0)
; #define G_BAR() do { asm volatile("s_waitcnt lgkmcnt(0)" ::: "memory"); __builtin_amdgcn_s_barrier(); asm volatile("" ::: "memory"); } while (0)
; __device__ __forceinline__ void gemm_kloop_light(f32x4 (&acc)[8][4], LAS unsigned char* lds, const GemmT& T, ...
;     ...
;     for (int t = 0; t < nt; ++t) { const int cur = t & 1; const bool w1 = t + 1 < nt, i2 = t + 2 < nt;
;         if (w1) { G_DMA_A(cur ^ 1, t + 1, 0); G_DMA_A(cur ^ 1, t + 1, 1); G_DMA_A(cur ^ 1, t + 1, 2); G_DMA_A(cur ^ 1, t + 1, 3); }
;         if (mlim > 0) {
; #pragma unroll
;             for (int ks = 0; ks < 2; ++ks) { const LAS unsigned char* s_ = lds + cur * 65536 + ks * 1024; bf16x8 Bf_[4];
; #pragma unroll
;                 for (int n_ = 0; n_ < 4; ++n_) Bf_[n_] = *(const LAS bf16x8*)(s_ + T.b_r + n_ * 2048);
; #pragma unroll
;                 for (int m_ = 0; m_ < 8; ++m_) if (m_ < mlim) { const bf16x8 At_ = *(const LAS bf16x8*)(s_ + T.a_r + m_ * 2048);
; #pragma unroll
;                     for (int n_ = 0; n_ < 4; ++n_) acc[m_][n_] = __builtin_amdgcn_mfma_f32_16x16x32_bf16(Bf_[n_], At_, acc[m_][n_], 0, 0, 0); } } }
;         if (w1) { G_RETIRE(); G_WRITE_B(cur ^ 1); }
;         if (i2) G_ISSUE_B(t + 2);
;         G_BAR(); }
.Lmy_d2d_bar:
	s_waitcnt lgkmcnt(0)
	s_add_i32 s72, s72, 0x80000
	s_add_i32 s3, s3, 0x10000
	s_addk_i32 s73, 0x80
	s_cmp_eq_u32 s72, 0x100e000
	s_barrier
	s_cbranch_scc1 .LBB0_1515

; #define G_DMA_A(buf, t, i_) __builtin_amdgcn_raw_ptr_buffer_load_lds(ra, (LAS void*)(lds + (buf) * 65536 + a_wu + (i_) * 8192), 16, ao##i_, (unsigned)(t) * 128u, 0, 0)
; #define G_ISSUE_B(t) do { const unsigned so_ = (unsigned)(t) * 64u * ldbB; _Pragma("unroll") for (int i_ = 0; i_ < 8; ++i_) sb[i_] = __builtin_bit_cast(f32x4, __builtin_amdgcn_raw_buffer_load_b128(rb, bo, so_ + (unsigned)i_ * ldbB, 0)); } while (0)
; #define G_RETIRE() asm volatile("s_waitcnt vmcnt(0)" : "+v"(sb[0]), "+v"(sb[1]), "+v"(sb[2]), "+v"(sb[3]), "+v"(sb[4]), "+v"(sb[5]), "+v"(sb[6]), "+v"(sb[7]) :: "memory")
; #define G_WRITE_B(buf) do { LAS unsigned char* d_ = lds + (buf) * 65536; \
;         _Pragma("unroll") for (int j_ = 0; j_ < 4; ++j_) { u32x4 w_; w_.x = cvtpk(sb[0][j_], sb[1][j_]); w_.y = cvtpk(sb[2][j_], sb[3][j_]); w_.z = cvtpk(sb[4][j_], sb[5][j_]); w_.w = cvtpk(sb[6][j_], sb[7][j_]); \
;             *(LAS u32x4*)(d_ + 32768 + T.b_w + ((T.b_rot + 64u * j_) & 255u)) = w_; } } while (0)
; #define G_LDB(dst, buf, ks) do { const LAS unsigned char* s_ = lds + (buf) * 65536 + (ks) * 1024; _Pragma("unroll") for (int n_ = 0; n_ < 4; ++n_) dst[n_] = *(const LAS bf16x8*)(s_ + T.b_r + n_ * 2048); } while (0)
; #define G_LDA(dst, buf, ks, h_) do { const LAS unsigned char* s_ = lds + (buf) * 65536 + (ks) * 1024; _Pragma("unroll") for (int m_ = 0; m_ < 4; ++m_) dst[m_] = *(const LAS bf16x8*)(s_ + T.a_r + ((h_) * 4 + m_) * 2048); } while (0)
; #define G_SB() __builtin_amdgcn_sched_barrier(0)
; #define G_BAR() do { asm volatile("s_waitcnt lgkmcnt(0)" ::: "memory"); __builtin_amdgcn_s_barrier(); asm volatile("" ::: "memory"); } while (0)
; __device__ __forceinline__ void gemm_kloop(f32x4 (&acc)[8][4], LAS unsigned char* lds, const GemmT& T, ...
;     ...
;     for (int t = 0; t < nt; ++t) { const int cur = t & 1; const bool w1 = t + 1 < nt, i2 = t + 2 < nt;
;         G_LDB(Bf0, cur, 0); G_LDA(AtA, cur, 0, 0); G_SB();
;         G_LDA(AtB, cur, 0, 1); if (w1) { G_DMA_A(cur ^ 1, t + 1, 0); G_DMA_A(cur ^ 1, t + 1, 1); G_DMA_A(cur ^ 1, t + 1, 2); G_DMA_A(cur ^ 1, t + 1, 3); } G_MMA(AtA, Bf0, 0); G_SB();
;         G_LDB(Bf1, cur, 1); G_LDA(AtA, cur, 1, 0); G_MMA(AtB, Bf0, 1); G_SB();
;         G_LDA(AtB, cur, 1, 1); if (w1) { G_RETIRE(); G_WRITE_B(cur ^ 1); } if (i2) G_ISSUE_B(t + 2); G_MMA(AtA, Bf1, 0); G_SB();
;         G_MMA(AtB, Bf1, 1); G_SB();
;         G_BAR(); }
.Lmy_eldc:
	s_waitcnt vmcnt(0)
	s_add_i32 s6, s3, 0xffff2000
	s_waitcnt lgkmcnt(3)
	v_mfma_f32_16x16x32_bf16 v[160:163], v[164:167], v[176:179], v[160:163]
	v_cvt_pk_bf16_f32 v230, v5, v9
	v_cvt_pk_bf16_f32 v234, v6, v10
	s_add_i32 s7, s3, 0xffff4000
	v_mfma_f32_16x16x32_bf16 v[156:159], v[168:171], v[176:179], v[156:159]
	v_cvt_pk_bf16_f32 v231, v13, v17
	v_cvt_pk_bf16_f32 v235, v14, v18
	v_cvt_pk_bf16_f32 v232, v21, v29
	v_mfma_f32_16x16x32_bf16 v[152:155], v[180:183], v[176:179], v[152:155]
	v_cvt_pk_bf16_f32 v236, v22, v30
	v_cvt_pk_bf16_f32 v233, v25, v33
	v_cvt_pk_bf16_f32 v237, v26, v34
	v_mfma_f32_16x16x32_bf16 v[148:151], v[184:187], v[176:179], v[148:151]
	v_cvt_pk_bf16_f32 v172, v4, v8
	v_cvt_pk_bf16_f32 v173, v12, v16
	v_cvt_pk_bf16_f32 v174, v20, v28
	s_waitcnt lgkmcnt(2)
	v_mfma_f32_16x16x32_bf16 v[144:147], v[164:167], v[200:203], v[144:147]
	v_cvt_pk_bf16_f32 v175, v24, v32
	v_add_u32_e32 v3, s5, v228
	v_mfma_f32_16x16x32_bf16 v[140:143], v[168:171], v[200:203], v[140:143]
	v_mfma_f32_16x16x32_bf16 v[136:139], v[180:183], v[200:203], v[136:139]
	v_mfma_f32_16x16x32_bf16 v[132:135], v[184:187], v[200:203], v[132:135]
	v_cvt_pk_bf16_f32 v188, v7, v11
	buffer_load_dwordx4 v[4:7], v222, s[24:27], s6 offen
	buffer_load_dwordx4 v[8:11], v222, s[24:27], s7 offen
	s_add_i32 s6, s3, 0xffff6000
	v_cvt_pk_bf16_f32 v189, v15, v19
	s_add_i32 s7, s3, 0xffff8000
	buffer_load_dwordx4 v[12:15], v222, s[24:27], s6 offen
	buffer_load_dwordx4 v[16:19], v222, s[24:27], s7 offen
	s_add_i32 s6, s3, 0xffffa000
	v_cvt_pk_bf16_f32 v190, v23, v31
	s_add_i32 s7, s3, 0xffffc000
	buffer_load_dwordx4 v[20:23], v222, s[24:27], s6 offen
	buffer_load_dwordx4 v[28:31], v222, s[24:27], s7 offen
	s_add_i32 s6, s3, 0xffffe000
	v_cvt_pk_bf16_f32 v191, v27, v35
	buffer_load_dwordx4 v[24:27], v222, s[24:27], s6 offen
	buffer_load_dwordx4 v[32:35], v222, s[24:27], s3 offen
	s_waitcnt lgkmcnt(1)
	v_mfma_f32_16x16x32_bf16 v[128:131], v[164:167], v[204:207], v[128:131]
	v_mfma_f32_16x16x32_bf16 v[124:127], v[168:171], v[204:207], v[124:127]
	v_mfma_f32_16x16x32_bf16 v[120:123], v[180:183], v[204:207], v[120:123]
	v_mfma_f32_16x16x32_bf16 v[116:119], v[184:187], v[204:207], v[116:119]
	v_add_u32_e32 v192, v3, v219
	v_add_u32_e32 v3, v3, v221
	ds_write_b128 v192, v[172:175] offset:32768
	ds_write_b128 v192, v[230:233] offset:32832
	s_waitcnt lgkmcnt(2)
	v_mfma_f32_16x16x32_bf16 v[112:115], v[164:167], v[208:211], v[112:115]
	ds_write_b128 v192, v[234:237] offset:32896
	ds_write_b128 v3, v[188:191] offset:32768
	v_mfma_f32_16x16x32_bf16 v[108:111], v[168:171], v[208:211], v[108:111]
	v_mfma_f32_16x16x32_bf16 v[104:107], v[180:183], v[208:211], v[104:107]
	v_mfma_f32_16x16x32_bf16 v[100:103], v[184:187], v[208:211], v[100:103]
	s_waitcnt lgkmcnt(0)
	s_add_i32 s3, s3, 0x80000
	s_addk_i32 s4, 0x80
	s_add_i32 s2, s2, 0x10000
	s_cmp_lg_u32 s3, 0x100e000
	s_barrier
	s_cbranch_scc1 .LBB0_1576
	v_add_u32_e32 v3, 0, v227
	v_add_u32_e32 v204, 0, v217
	ds_read_b128 v[164:167], v3 offset:32768
	ds_read_b128 v[168:171], v3 offset:34816
	ds_read_b128 v[172:175], v3 offset:36864
	ds_read_b128 v[176:179], v3 offset:38912
	ds_read_b128 v[180:183], v204
	ds_read_b128 v[184:187], v204 offset:2048
	ds_read_b128 v[188:191], v204 offset:4096
	ds_read_b128 v[192:195], v204 offset:6144
	s_add_i32 m0, s1, 0x10000
	s_add_i32 s2, s1, 0x16000
	s_add_i32 s3, s1, 0x14000
	s_add_i32 s1, s1, 0x12000
	s_mov_b32 s38, s26
	s_mov_b32 s39, s27
	s_waitcnt lgkmcnt(3)
	v_mfma_f32_16x16x32_bf16 v[160:163], v[164:167], v[180:183], v[160:163]
	v_mfma_f32_16x16x32_bf16 v[156:159], v[168:171], v[180:183], v[156:159]
	v_mfma_f32_16x16x32_bf16 v[152:155], v[172:175], v[180:183], v[152:155]
	v_mfma_f32_16x16x32_bf16 v[148:151], v[176:179], v[180:183], v[148:151]
	s_waitcnt lgkmcnt(2)
	v_mfma_f32_16x16x32_bf16 v[144:147], v[164:167], v[184:187], v[144:147]
	v_mfma_f32_16x16x32_bf16 v[140:143], v[168:171], v[184:187], v[140:143]
	v_mfma_f32_16x16x32_bf16 v[136:139], v[172:175], v[184:187], v[136:139]
	v_mfma_f32_16x16x32_bf16 v[132:135], v[176:179], v[184:187], v[132:135]
	ds_read_b128 v[180:183], v204 offset:8192
	ds_read_b128 v[184:187], v204 offset:10240
	ds_read_b128 v[196:199], v204 offset:12288
	ds_read_b128 v[200:203], v204 offset:14336
	buffer_load_dwordx4 v225, s[36:39], s79 offen lds
	s_mov_b32 m0, s1
	s_waitcnt lgkmcnt(4)
	v_mfma_f32_16x16x32_bf16 v[108:111], v[168:171], v[192:195], v[108:111]
	buffer_load_dwordx4 v226, s[36:39], s79 offen lds
	s_mov_b32 m0, s3
	s_nop 0
	buffer_load_dwordx4 v224, s[36:39], s79 offen lds
	s_mov_b32 m0, s2
	v_mfma_f32_16x16x32_bf16 v[104:107], v[172:175], v[192:195], v[104:107]
	buffer_load_dwordx4 v223, s[36:39], s79 offen lds
	v_mfma_f32_16x16x32_bf16 v[100:103], v[176:179], v[192:195], v[100:103]
	v_mfma_f32_16x16x32_bf16 v[128:131], v[164:167], v[188:191], v[128:131]
	v_mfma_f32_16x16x32_bf16 v[124:127], v[168:171], v[188:191], v[124:127]
	v_mfma_f32_16x16x32_bf16 v[120:123], v[172:175], v[188:191], v[120:123]
	v_mfma_f32_16x16x32_bf16 v[116:119], v[176:179], v[188:191], v[116:119]
	v_mfma_f32_16x16x32_bf16 v[112:115], v[164:167], v[192:195], v[112:115]
	s_waitcnt lgkmcnt(3)
	v_mfma_f32_16x16x32_bf16 v[96:99], v[164:167], v[180:183], v[96:99]
	v_mfma_f32_16x16x32_bf16 v[92:95], v[168:171], v[180:183], v[92:95]
	v_mfma_f32_16x16x32_bf16 v[88:91], v[172:175], v[180:183], v[88:91]
	v_mfma_f32_16x16x32_bf16 v[84:87], v[176:179], v[180:183], v[84:87]
	s_waitcnt lgkmcnt(2)
	v_mfma_f32_16x16x32_bf16 v[80:83], v[164:167], v[184:187], v[80:83]
	v_mfma_f32_16x16x32_bf16 v[76:79], v[168:171], v[184:187], v[76:79]
	v_mfma_f32_16x16x32_bf16 v[72:75], v[172:175], v[184:187], v[72:75]
	v_mfma_f32_16x16x32_bf16 v[68:71], v[176:179], v[184:187], v[68:71]
	s_waitcnt lgkmcnt(1)
; #define G_DMA_A(buf, t, i_) __builtin_amdgcn_raw_ptr_buffer_load_lds(ra, (LAS void*)(lds + (buf) * 65536 + a_wu + (i_) * 8192), 16, ao##i_, (unsigned)(t) * 128u, 0, 0)
; #define G_ISSUE_B(t) do { const unsigned so_ = (unsigned)(t) * 64u * ldbB; _Pragma("unroll") for (int i_ = 0; i_ < 8; ++i_) sb[i_] = __builtin_bit_cast(f32x4, __builtin_amdgcn_raw_buffer_load_b128(rb, bo, so_ + (unsigned)i_ * ldbB, 0)); } while (0)
; #define G_RETIRE() asm volatile("s_waitcnt vmcnt(0)" : "+v"(sb[0]), "+v"(sb[1]), "+v"(sb[2]), "+v"(sb[3]), "+v"(sb[4]), "+v"(sb[5]), "+v"(sb[6]), "+v"(sb[7]) :: "memory")
; #define G_WRITE_B(buf) do { LAS unsigned char* d_ = lds + (buf) * 65536; \
;         _Pragma("unroll") for (int j_ = 0; j_ < 4; ++j_) { u32x4 w_; w_.x = cvtpk(sb[0][j_], sb[1][j_]); w_.y = cvtpk(sb[2][j_], sb[3][j_]); w_.z = cvtpk(sb[4][j_], sb[5][j_]); w_.w = cvtpk(sb[6][j_], sb[7][j_]); \
;             *(LAS u32x4*)(d_ + 32768 + T.b_w + ((T.b_rot + 64u * j_) & 255u)) = w_; } } while (0)
; #define G_LDB(dst, buf, ks) do { const LAS unsigned char* s_ = lds + (buf) * 65536 + (ks) * 1024; _Pragma("unroll") for (int n_ = 0; n_ < 4; ++n_) dst[n_] = *(const LAS bf16x8*)(s_ + T.b_r + n_ * 2048); } while (0)
; #define G_LDA(dst, buf, ks, h_) do { const LAS unsigned char* s_ = lds + (buf) * 65536 + (ks) * 1024; _Pragma("unroll") for (int m_ = 0; m_ < 4; ++m_) dst[m_] = *(const LAS bf16x8*)(s_ + T.a_r + ((h_) * 4 + m_) * 2048); } while (0)
; #define G_SB() __builtin_amdgcn_sched_barrier(0)
; #define G_BAR() do { asm volatile("s_waitcnt lgkmcnt(0)" ::: "memory"); __builtin_amdgcn_s_barrier(); asm volatile("" ::: "memory"); } while (0)
; __device__ __forceinline__ void gemm_kloop(f32x4 (&acc)[8][4], LAS unsigned char* lds, const GemmT& T, ...
;     ...
;     for (int t = 0; t < nt; ++t) { const int cur = t & 1; const bool w1 = t + 1 < nt, i2 = t + 2 < nt;
;         G_LDB(Bf0, cur, 0); G_LDA(AtA, cur, 0, 0); G_SB();
;         G_LDA(AtB, cur, 0, 1); if (w1) { G_DMA_A(cur ^ 1, t + 1, 0); G_DMA_A(cur ^ 1, t + 1, 1); G_DMA_A(cur ^ 1, t + 1, 2); G_DMA_A(cur ^ 1, t + 1, 3); } G_MMA(AtA, Bf0, 0); G_SB();
;         G_LDB(Bf1, cur, 1); G_LDA(AtA, cur, 1, 0); G_MMA(AtB, Bf0, 1); G_SB();
;         G_LDA(AtB, cur, 1, 1); if (w1) { G_RETIRE(); G_WRITE_B(cur ^ 1); } if (i2) G_ISSUE_B(t + 2); G_MMA(AtA, Bf1, 0); G_SB();
;         G_MMA(AtB, Bf1, 1); G_SB();
;         G_BAR(); }
	v_mfma_f32_16x16x32_bf16 v[64:67], v[164:167], v[196:199], v[64:67]
	v_mfma_f32_16x16x32_bf16 v[60:63], v[168:171], v[196:199], v[60:63]
	v_mfma_f32_16x16x32_bf16 v[56:59], v[172:175], v[196:199], v[56:59]
	v_mfma_f32_16x16x32_bf16 v[52:55], v[176:179], v[196:199], v[52:55]
	s_waitcnt lgkmcnt(0)
	v_mfma_f32_16x16x32_bf16 v[48:51], v[164:167], v[200:203], v[48:51]
	v_mfma_f32_16x16x32_bf16 v[44:47], v[168:171], v[200:203], v[44:47]
	ds_read_b128 v[164:167], v3 offset:33792
	ds_read_b128 v[168:171], v3 offset:35840
	ds_read_b128 v[180:183], v3 offset:37888
	ds_read_b128 v[184:187], v3 offset:39936
	v_mfma_f32_16x16x32_bf16 v[40:43], v[172:175], v[200:203], v[40:43]
	ds_read_b128 v[172:175], v204 offset:1024
	ds_read_b128 v[188:191], v204 offset:3072
	ds_read_b128 v[192:195], v204 offset:5120
	ds_read_b128 v[196:199], v204 offset:7168
	v_mfma_f32_16x16x32_bf16 v[36:39], v[176:179], v[200:203], v[36:39]
	s_waitcnt lgkmcnt(3)
	v_mfma_f32_16x16x32_bf16 v[160:163], v[164:167], v[172:175], v[160:163]
	v_add_u32_e32 v3, s29, v220
	v_mfma_f32_16x16x32_bf16 v[156:159], v[168:171], v[172:175], v[156:159]
	v_mfma_f32_16x16x32_bf16 v[152:155], v[180:183], v[172:175], v[152:155]
	v_mfma_f32_16x16x32_bf16 v[148:151], v[184:187], v[172:175], v[148:151]
	ds_read_b128 v[172:175], v204 offset:9216
	ds_read_b128 v[176:179], v204 offset:11264
	ds_read_b128 v[200:203], v204 offset:13312
	ds_read_b128 v[204:207], v204 offset:15360
	s_waitcnt vmcnt(4)
	s_waitcnt vmcnt(0)
	s_waitcnt lgkmcnt(6)
	v_mfma_f32_16x16x32_bf16 v[144:147], v[164:167], v[188:191], v[144:147]
	v_mfma_f32_16x16x32_bf16 v[140:143], v[168:171], v[188:191], v[140:143]
	v_mfma_f32_16x16x32_bf16 v[136:139], v[180:183], v[188:191], v[136:139]
	v_mfma_f32_16x16x32_bf16 v[132:135], v[184:187], v[188:191], v[132:135]
	v_cvt_pk_bf16_f32 v188, v4, v8
	v_cvt_pk_bf16_f32 v189, v12, v16
	v_cvt_pk_bf16_f32 v190, v20, v28
	v_cvt_pk_bf16_f32 v191, v24, v32
	v_add_u32_e32 v4, v3, v219
	ds_write_b128 v4, v[188:191]
	v_cvt_pk_bf16_f32 v188, v5, v9
	v_cvt_pk_bf16_f32 v189, v13, v17
	v_cvt_pk_bf16_f32 v190, v21, v29
	v_cvt_pk_bf16_f32 v191, v25, v33
	ds_write_b128 v4, v[188:191] offset:64
	v_cvt_pk_bf16_f32 v188, v6, v10
	v_cvt_pk_bf16_f32 v189, v14, v18
	v_cvt_pk_bf16_f32 v190, v22, v30
	v_cvt_pk_bf16_f32 v191, v26, v34
	ds_write_b128 v4, v[188:191] offset:128
	v_cvt_pk_bf16_f32 v4, v7, v11
	v_cvt_pk_bf16_f32 v5, v15, v19
	v_cvt_pk_bf16_f32 v6, v23, v31
	v_cvt_pk_bf16_f32 v7, v27, v35
	v_add_u32_e32 v3, v3, v221
	s_waitcnt lgkmcnt(7)
	v_mfma_f32_16x16x32_bf16 v[108:111], v[168:171], v[196:199], v[108:111]
	ds_write_b128 v3, v[4:7]
	v_mfma_f32_16x16x32_bf16 v[8:11], v[180:183], v[196:199], v[104:107]
	v_mfma_f32_16x16x32_bf16 v[4:7], v[184:187], v[196:199], v[100:103]
	v_mfma_f32_16x16x32_bf16 v[128:131], v[164:167], v[192:195], v[128:131]
	v_mfma_f32_16x16x32_bf16 v[124:127], v[168:171], v[192:195], v[124:127]
	v_mfma_f32_16x16x32_bf16 v[120:123], v[180:183], v[192:195], v[120:123]
	v_mfma_f32_16x16x32_bf16 v[116:119], v[184:187], v[192:195], v[116:119]
	v_mfma_f32_16x16x32_bf16 v[112:115], v[164:167], v[196:199], v[112:115]
	s_waitcnt lgkmcnt(7)
	v_mfma_f32_16x16x32_bf16 v[12:15], v[164:167], v[172:175], v[96:99]
	v_mfma_f32_16x16x32_bf16 v[16:19], v[168:171], v[172:175], v[92:95]
	v_mfma_f32_16x16x32_bf16 v[20:23], v[180:183], v[172:175], v[88:91]
	v_mfma_f32_16x16x32_bf16 v[24:27], v[184:187], v[172:175], v[84:87]
	s_waitcnt lgkmcnt(6)
	v_mfma_f32_16x16x32_bf16 v[28:31], v[164:167], v[176:179], v[80:83]
	v_mfma_f32_16x16x32_bf16 v[32:35], v[168:171], v[176:179], v[76:79]
	v_mfma_f32_16x16x32_bf16 v[72:75], v[180:183], v[176:179], v[72:75]
	v_mfma_f32_16x16x32_bf16 v[68:71], v[184:187], v[176:179], v[68:71]
	s_waitcnt lgkmcnt(5)
	v_mfma_f32_16x16x32_bf16 v[64:67], v[164:167], v[200:203], v[64:67]
	v_mfma_f32_16x16x32_bf16 v[60:63], v[168:171], v[200:203], v[60:63]
	v_mfma_f32_16x16x32_bf16 v[56:59], v[180:183], v[200:203], v[56:59]
	v_mfma_f32_16x16x32_bf16 v[52:55], v[184:187], v[200:203], v[52:55]
	s_waitcnt lgkmcnt(4)
	v_mfma_f32_16x16x32_bf16 v[48:51], v[164:167], v[204:207], v[48:51]
	v_mfma_f32_16x16x32_bf16 v[44:47], v[168:171], v[204:207], v[44:47]
	v_mfma_f32_16x16x32_bf16 v[40:43], v[180:183], v[204:207], v[40:43]
	v_mfma_f32_16x16x32_bf16 v[36:39], v[184:187], v[204:207], v[36:39]
	s_add_i32 s1, 0, 0x10000
	s_waitcnt lgkmcnt(0)
	s_barrier
; #define G_DMA_A(buf, t, i_) __builtin_amdgcn_raw_ptr_buffer_load_lds(ra, (LAS void*)(lds + (buf) * 65536 + a_wu + (i_) * 8192), 16, ao##i_, (unsigned)(t) * 128u, 0, 0)
; #define G_ISSUE_B(t) do { const unsigned so_ = (unsigned)(t) * 64u * ldbB; _Pragma("unroll") for (int i_ = 0; i_ < 8; ++i_) sb[i_] = __builtin_bit_cast(f32x4, __builtin_amdgcn_raw_buffer_load_b128(rb, bo, so_ + (unsigned)i_ * ldbB, 0)); } while (0)
; #define G_RETIRE() asm volatile("s_waitcnt vmcnt(0)" : "+v"(sb[0]), "+v"(sb[1]), "+v"(sb[2]), "+v"(sb[3]), "+v"(sb[4]), "+v"(sb[5]), "+v"(sb[6]), "+v"(sb[7]) :: "memory")
; #define G_WRITE_B(buf) do { LAS unsigned char* d_ = lds + (buf) * 65536; \
;         _Pragma("unroll") for (int j_ = 0; j_ < 4; ++j_) { u32x4 w_; w_.x = cvtpk(sb[0][j_], sb[1][j_]); w_.y = cvtpk(sb[2][j_], sb[3][j_]); w_.z = cvtpk(sb[4][j_], sb[5][j_]); w_.w = cvtpk(sb[6][j_], sb[7][j_]); \
;             *(LAS u32x4*)(d_ + 32768 + T.b_w + ((T.b_rot + 64u * j_) & 255u)) = w_; } } while (0)
; #define G_LDB(dst, buf, ks) do { const LAS unsigned char* s_ = lds + (buf) * 65536 + (ks) * 1024; _Pragma("unroll") for (int n_ = 0; n_ < 4; ++n_) dst[n_] = *(const LAS bf16x8*)(s_ + T.b_r + n_ * 2048); } while (0)
; #define G_LDA(dst, buf, ks, h_) do { const LAS unsigned char* s_ = lds + (buf) * 65536 + (ks) * 1024; _Pragma("unroll") for (int m_ = 0; m_ < 4; ++m_) dst[m_] = *(const LAS bf16x8*)(s_ + T.a_r + ((h_) * 4 + m_) * 2048); } while (0)
; #define G_SB() __builtin_amdgcn_sched_barrier(0)
; #define G_BAR() do { asm volatile("s_waitcnt lgkmcnt(0)" ::: "memory"); __builtin_amdgcn_s_barrier(); asm volatile("" ::: "memory"); } while (0)
; __device__ __forceinline__ void gemm_kloop(f32x4 (&acc)[8][4], LAS unsigned char* lds, const GemmT& T, ...
;     ...
;     for (int t = 0; t < nt; ++t) { const int cur = t & 1; const bool w1 = t + 1 < nt, i2 = t + 2 < nt;
;         G_LDB(Bf0, cur, 0); G_LDA(AtA, cur, 0, 0); G_SB();
;         G_LDA(AtB, cur, 0, 1); if (w1) { G_DMA_A(cur ^ 1, t + 1, 0); G_DMA_A(cur ^ 1, t + 1, 1); G_DMA_A(cur ^ 1, t + 1, 2); G_DMA_A(cur ^ 1, t + 1, 3); } G_MMA(AtA, Bf0, 0); G_SB();
;         G_LDB(Bf1, cur, 1); G_LDA(AtA, cur, 1, 0); G_MMA(AtB, Bf0, 1); G_SB();
;         G_LDA(AtB, cur, 1, 1); if (w1) { G_RETIRE(); G_WRITE_B(cur ^ 1); } if (i2) G_ISSUE_B(t + 2); G_MMA(AtA, Bf1, 0); G_SB();
;         G_MMA(AtB, Bf1, 1); G_SB();
;         G_BAR(); }
	v_add_u32_e32 v3, s1, v218
	ds_read_b128 v[76:79], v3
	ds_read_b128 v[80:83], v3 offset:2048
	ds_read_b128 v[84:87], v3 offset:4096
	ds_read_b128 v[88:91], v3 offset:6144
	v_add_u32_e32 v3, s1, v217
	ds_read_b128 v[92:95], v3
	ds_read_b128 v[96:99], v3 offset:2048
	ds_read_b128 v[100:103], v3 offset:4096
	ds_read_b128 v[104:107], v3 offset:6144
	s_waitcnt lgkmcnt(2)
	v_mfma_f32_16x16x32_bf16 v[144:147], v[76:79], v[96:99], v[144:147]
	v_mfma_f32_16x16x32_bf16 v[140:143], v[80:83], v[96:99], v[140:143]
	v_mfma_f32_16x16x32_bf16 v[170:173], v[84:87], v[96:99], v[136:139]
	v_mfma_f32_16x16x32_bf16 v[96:99], v[88:91], v[96:99], v[132:135]
	s_waitcnt lgkmcnt(1)
	v_mfma_f32_16x16x32_bf16 v[128:131], v[76:79], v[100:103], v[128:131]
	v_mfma_f32_16x16x32_bf16 v[124:127], v[80:83], v[100:103], v[124:127]
	v_mfma_f32_16x16x32_bf16 v[120:123], v[84:87], v[100:103], v[120:123]
	v_mfma_f32_16x16x32_bf16 v[116:119], v[88:91], v[100:103], v[116:119]
	s_waitcnt lgkmcnt(0)
	v_mfma_f32_16x16x32_bf16 v[174:177], v[80:83], v[104:107], v[108:111]
	ds_read_b128 v[100:103], v3 offset:8192
	s_nop 1
	ds_read_b128 v[108:111], v3 offset:10240
	ds_read_b128 v[132:135], v3 offset:12288
	ds_read_b128 v[136:139], v3 offset:14336
	v_mfma_f32_16x16x32_bf16 v[160:163], v[76:79], v[92:95], v[160:163]
	v_mfma_f32_16x16x32_bf16 v[164:167], v[80:83], v[92:95], v[156:159]
	v_mfma_f32_16x16x32_bf16 v[152:155], v[84:87], v[92:95], v[152:155]
	v_mfma_f32_16x16x32_bf16 v[92:95], v[88:91], v[92:95], v[148:151]
	v_mfma_f32_16x16x32_bf16 v[8:11], v[84:87], v[104:107], v[8:11]
	v_mfma_f32_16x16x32_bf16 v[4:7], v[88:91], v[104:107], v[4:7]
	v_mfma_f32_16x16x32_bf16 v[112:115], v[76:79], v[104:107], v[112:115]
	v_add_u32_e32 v3, s64, v218
	ds_read_b128 v[206:209], v3
	ds_read_b128 v[210:213], v3 offset:2048
	ds_read_b128 v[222:225], v3 offset:4096
	ds_read_b128 v[226:229], v3 offset:6144
	v_add_u32_e32 v3, s64, v217
	s_waitcnt lgkmcnt(5)
	v_mfma_f32_16x16x32_bf16 v[198:201], v[88:91], v[132:135], v[52:55]
	s_waitcnt lgkmcnt(4)
	v_mfma_f32_16x16x32_bf16 v[202:205], v[76:79], v[136:139], v[48:51]
	v_mfma_f32_16x16x32_bf16 v[218:221], v[80:83], v[136:139], v[44:47]
	v_mfma_f32_16x16x32_bf16 v[230:233], v[84:87], v[136:139], v[40:43]
	s_nop 2
	ds_read_b128 v[40:43], v3
	ds_read_b128 v[44:47], v3 offset:2048
	ds_read_b128 v[48:51], v3 offset:4096
	ds_read_b128 v[52:55], v3 offset:6144
	v_mfma_f32_16x16x32_bf16 v[12:15], v[76:79], v[100:103], v[12:15]
	v_mfma_f32_16x16x32_bf16 v[16:19], v[80:83], v[100:103], v[16:19]
	v_mfma_f32_16x16x32_bf16 v[20:23], v[84:87], v[100:103], v[20:23]
	v_mfma_f32_16x16x32_bf16 v[24:27], v[88:91], v[100:103], v[24:27]
	v_mfma_f32_16x16x32_bf16 v[28:31], v[76:79], v[108:111], v[28:31]
	v_mfma_f32_16x16x32_bf16 v[32:35], v[80:83], v[108:111], v[32:35]
	v_mfma_f32_16x16x32_bf16 v[178:181], v[84:87], v[108:111], v[72:75]
	v_mfma_f32_16x16x32_bf16 v[182:185], v[88:91], v[108:111], v[68:71]
	v_mfma_f32_16x16x32_bf16 v[186:189], v[76:79], v[132:135], v[64:67]
	v_mfma_f32_16x16x32_bf16 v[190:193], v[80:83], v[132:135], v[60:63]
	v_mfma_f32_16x16x32_bf16 v[194:197], v[84:87], v[132:135], v[56:59]
	v_mfma_f32_16x16x32_bf16 v[234:237], v[88:91], v[136:139], v[36:39]
	s_waitcnt lgkmcnt(3)
	v_mfma_f32_16x16x32_bf16 v[158:161], v[206:209], v[40:43], v[160:163]
	v_mfma_f32_16x16x32_bf16 v[166:169], v[210:213], v[40:43], v[164:167]
	v_mfma_f32_16x16x32_bf16 v[150:153], v[222:225], v[40:43], v[152:155]
	v_mfma_f32_16x16x32_bf16 v[154:157], v[226:229], v[40:43], v[92:95]
	s_waitcnt lgkmcnt(2)
	v_mfma_f32_16x16x32_bf16 v[134:137], v[206:209], v[44:47], v[144:147]
	v_mfma_f32_16x16x32_bf16 v[146:149], v[210:213], v[44:47], v[140:143]
	v_mfma_f32_16x16x32_bf16 v[102:105], v[222:225], v[44:47], v[170:173]
	v_mfma_f32_16x16x32_bf16 v[106:109], v[226:229], v[44:47], v[96:99]
	s_waitcnt lgkmcnt(1)
	v_mfma_f32_16x16x32_bf16 v[90:93], v[226:229], v[48:51], v[116:119]
	s_waitcnt lgkmcnt(0)
	v_mfma_f32_16x16x32_bf16 v[78:81], v[206:209], v[52:55], v[112:115]
	v_mfma_f32_16x16x32_bf16 v[70:73], v[222:225], v[52:55], v[8:11]
	s_nop 2
	ds_read_b128 v[8:11], v3 offset:8192
	ds_read_b128 v[42:45], v3 offset:10240
	ds_read_b128 v[110:113], v3 offset:12288
	ds_read_b128 v[114:117], v3 offset:14336
	v_mfma_f32_16x16x32_bf16 v[94:97], v[206:209], v[48:51], v[128:131]
	v_mfma_f32_16x16x32_bf16 v[98:101], v[210:213], v[48:51], v[124:127]
	v_mfma_f32_16x16x32_bf16 v[86:89], v[222:225], v[48:51], v[120:123]
	v_mfma_f32_16x16x32_bf16 v[82:85], v[210:213], v[52:55], v[174:177]
	v_mfma_f32_16x16x32_bf16 v[74:77], v[226:229], v[52:55], v[4:7]
	s_waitcnt lgkmcnt(3)
	v_mfma_f32_16x16x32_bf16 v[62:65], v[206:209], v[8:11], v[12:15]
	v_mfma_f32_16x16x32_bf16 v[66:69], v[210:213], v[8:11], v[16:19]
	v_mfma_f32_16x16x32_bf16 v[54:57], v[222:225], v[8:11], v[20:23]
	v_mfma_f32_16x16x32_bf16 v[58:61], v[226:229], v[8:11], v[24:27]
	s_waitcnt lgkmcnt(2)
	v_mfma_f32_16x16x32_bf16 v[46:49], v[206:209], v[42:45], v[28:31]
	v_mfma_f32_16x16x32_bf16 v[50:53], v[210:213], v[42:45], v[32:35]
	v_mfma_f32_16x16x32_bf16 v[38:41], v[222:225], v[42:45], v[178:181]
	v_mfma_f32_16x16x32_bf16 v[42:45], v[226:229], v[42:45], v[182:185]
	s_waitcnt lgkmcnt(1)
	v_mfma_f32_16x16x32_bf16 v[30:33], v[206:209], v[110:113], v[186:189]
	v_mfma_f32_16x16x32_bf16 v[34:37], v[210:213], v[110:113], v[190:193]
	v_mfma_f32_16x16x32_bf16 v[22:25], v[222:225], v[110:113], v[194:197]
	v_mfma_f32_16x16x32_bf16 v[26:29], v[226:229], v[110:113], v[198:201]
	s_waitcnt lgkmcnt(0)
	v_mfma_f32_16x16x32_bf16 v[14:17], v[206:209], v[114:117], v[202:205]
	v_mfma_f32_16x16x32_bf16 v[18:21], v[210:213], v[114:117], v[218:221]
	v_mfma_f32_16x16x32_bf16 v[6:9], v[222:225], v[114:117], v[230:233]
	v_mfma_f32_16x16x32_bf16 v[10:13], v[226:229], v[114:117], v[234:237]
	s_waitcnt lgkmcnt(0)
	s_barrier
